# baseline (speedup 1.0000x reference)
_Z13attn11_kernelILi4EEvPc:
	s_ashr_i32 s5, s2, 3
	s_load_dwordx2 s[12:13], s[0:1], 0x0
	s_lshr_b32 s4, s5, 29
	s_lshl_b32 s3, s2, 4
	s_add_i32 s6, s5, s4
	s_and_b32 s3, s3, 0x70
	s_ashr_i32 s4, s6, 3
	s_add_i32 s4, s3, s4
	s_and_b32 s3, s6, 0x1fffff8
	s_sub_i32 s3, s5, s3
	v_lshrrev_b32_e32 v1, 6, v0
	s_waitcnt lgkmcnt(0)
	s_add_u32 s14, s12, 0x2500000
	v_lshlrev_b32_e32 v192, 5, v1
	s_addc_u32 s15, s13, 0
	s_ashr_i32 s5, s4, 31
	s_mul_i32 s6, s4, 0x12000
	v_lshl_or_b32 v172, s3, 7, v192
	s_mul_hi_i32 s3, s4, 0x12000
	s_add_u32 s8, s14, s6
	s_addc_u32 s9, s15, s3
	s_add_u32 s16, s12, 0x3700000
	v_lshlrev_b32_e32 v169, 4, v0
	s_addc_u32 s17, s13, 0
	s_add_u32 s10, s16, s6
	v_add_u32_e32 v193, 0, v169
	v_lshrrev_b32_e32 v2, 2, v0
	v_bitop3_b32 v3, v169, 48, v0 bitop3:0x48
	s_addc_u32 s11, s17, s3
	s_mov_b64 s[46:47], s[8:9]
	s_mov_b64 s[48:49], s[10:11]
	s_mov_b64 s[50:51], s[14:15]
	s_mov_b64 s[52:53], s[16:17]
	v_readfirstlane_b32 s3, v193
	v_add_u32_e32 v4, 0x8000, v193
	v_lshl_or_b32 v170, v2, 6, v3
	v_mul_u32_u24_e32 v2, 0x480, v2
	v_mov_b32_e32 v171, 0
	s_mov_b32 m0, s3
	v_readfirstlane_b32 s3, v4
	v_add_u32_e32 v6, 0x2000, v193
	v_or_b32_e32 v2, v2, v3
	v_lshl_add_u64 v[174:175], s[8:9], 0, v[170:171]
	v_mov_b32_e32 v3, v171
	global_load_lds_dwordx4 v170, s[8:9]
	v_mov_b32_e32 v220, v170
	s_mov_b32 m0, s3
	s_mov_b64 s[8:9], 0x1000
	v_readfirstlane_b32 s6, v6
	v_add_u32_e32 v6, 0x4000, v193
	v_lshl_add_u64 v[176:177], s[10:11], 0, v[2:3]
	global_load_lds_dwordx4 v2, s[10:11]
	v_mov_b32_e32 v221, v2
	v_lshl_add_u64 v[4:5], v[174:175], 0, s[8:9]
	s_mov_b32 m0, s6
	s_mov_b64 s[10:11], 0x2000
	v_readfirstlane_b32 s6, v6
	v_add_u32_e32 v6, 0xa000, v193
	global_load_lds_dwordx4 v[4:5], off
	v_lshl_add_u64 v[4:5], v[174:175], 0, s[10:11]
	s_mov_b32 m0, s6
	v_readfirstlane_b32 s6, v6
	s_add_u32 s18, s12, 0x1500000
	global_load_lds_dwordx4 v[4:5], off
	v_lshl_add_u64 v[4:5], v[176:177], 0, 64
	s_mov_b32 m0, s6
	s_addc_u32 s19, s13, 0
	s_lshl_b64 s[20:21], s[4:5], 10
	v_ashrrev_i32_e32 v173, 31, v172
	v_and_b32_e32 v168, 31, v0
	global_load_lds_dwordx4 v[4:5], off
	v_lshl_add_u64 v[4:5], s[20:21], 0, v[172:173]
	v_or_b32_e32 v4, v4, v168
	v_lshlrev_b64 v[4:5], 6, v[4:5]
	v_lshl_add_u64 v[4:5], s[18:19], 0, v[4:5]
	v_and_b32_e32 v6, 32, v0
	v_mov_b32_e32 v7, v171
	v_lshl_add_u64 v[4:5], v[4:5], 0, v[6:7]
	global_load_dwordx4 v[152:155], v[4:5], off nt
	global_load_dwordx4 v[156:159], v[4:5], off offset:16 nt
	v_and_b32_e32 v4, 60, v0
	v_lshlrev_b32_e32 v5, 2, v0
	s_add_u32 s0, s0, 8
	s_movk_i32 s5, 0xa00
	v_lshlrev_b32_e32 v184, 7, v4
	v_or_b32_e32 v4, 64, v4
	v_bitop3_b32 v195, v5, v6, 48 bitop3:0x6c
	v_lshl_add_u64 v[178:179], s[14:15], 0, v[170:171]
	v_lshl_add_u64 v[180:181], s[16:17], 0, v[2:3]
	s_addc_u32 s1, s1, 0
	v_mad_u32_u24 v1, v1, s5, 0
	v_lshrrev_b32_e32 v2, 3, v0
	s_movk_i32 s5, 0x50
	v_and_b32_e32 v170, 48, v169
	v_bfe_u32 v0, v0, 2, 4
	v_lshrrev_b32_e32 v5, 2, v4
	v_mov_b32_e32 v144, 0x38383838
	v_bfe_u32 v226, v169, 6, 1
	v_bfe_u32 v227, v169, 8, 1
	v_cmp_eq_u32_e32 vcc, v226, v227
	s_nop 1
	v_cndmask_b32_e32 v144, 0, v144, vcc
	v_lshl_add_u64 v[182:183], s[18:19], 0, v[6:7]
	v_and_b32_e32 v2, 4, v2
	v_mad_u32_u24 v3, v168, s5, v1
	s_add_u32 s12, s12, 0x4900000
	v_add_u32_e32 v1, v1, v170
	v_mul_u32_u24_e32 v0, 0x50, v0
	v_mul_u32_u24_e32 v5, 0x50, v5
	s_movk_i32 s18, 0xffc0
	v_lshlrev_b32_e32 v199, 6, v168
	s_mov_b32 s7, 0
	s_movk_i32 s3, 0x2000
	s_movk_i32 s33, 0x4000
	v_mov_b32_e32 v173, 0x74747474
	v_mov_b32_e32 v194, 0x7f7f7f7f
	v_mov_b32_e32 v145, v144
	v_mov_b32_e32 v146, v144
	v_mov_b32_e32 v147, v144
	v_mov_b32_e32 v148, v144
	v_mov_b32_e32 v149, v144
	v_mov_b32_e32 v150, v144
	v_mov_b32_e32 v151, v144
	s_addc_u32 s13, s13, 0
	v_mov_b32_e32 v185, v171
	v_lshlrev_b32_e32 v186, 7, v4
	v_mov_b32_e32 v187, v171
	s_mov_b64 s[30:31], -1
	s_mov_b64 s[14:15], 0x3000
	s_mov_b64 s[16:17], 0xc0
	s_mov_b32 s19, -1
	s_mov_b32 s5, 0xff61b1e6
	s_mov_b32 s36, 0x41000000
	s_mov_b64 s[20:21], 0x80
	s_mov_b64 s[22:23], 0x11000
	s_mov_b64 s[24:25], 0x400
	s_mov_b64 s[26:27], 0x440
	s_mov_b32 s37, 0x42800000
	v_add_u32_e32 v196, v3, v2
	v_add_u32_e32 v197, v1, v0
	v_add_u32_e32 v198, v1, v5
	v_add_u32_e32 v197, 0x10000, v197
	v_add_u32_e32 v198, 0x10000, v198
	v_mov_b32_e32 v0, v171
	v_mov_b32_e32 v1, v171
	v_mov_b32_e32 v2, v171
	v_mov_b32_e32 v3, v171
	v_mov_b32_e32 v4, v171
	v_mov_b32_e32 v5, v171
	v_mov_b32_e32 v6, v171
	v_mov_b32_e32 v8, v171
	v_mov_b32_e32 v9, v171
	v_mov_b32_e32 v10, v171
	v_mov_b32_e32 v11, v171
	v_mov_b32_e32 v12, v171
	v_mov_b32_e32 v13, v171
	v_mov_b32_e32 v14, v171
	v_mov_b32_e32 v15, v171
	s_mov_b32 s38, 0
	v_mov_b32_e32 v160, v171
	v_mov_b32_e32 v161, v171
	v_mov_b32_e32 v162, v171
	v_mov_b32_e32 v163, v171
	v_mov_b32_e32 v164, v171
	v_mov_b32_e32 v165, v171
	v_mov_b32_e32 v166, v171
	v_mov_b32_e32 v167, v171
	v_xor_b32_e32 v200, 16, v195
	v_add_u32_e32 v201, 0, v199
	v_add_u32_e32 v222, v199, v195
	v_add_u32_e32 v223, v199, v200
	v_readfirstlane_b32 s40, v169
	v_add_u32_e32 v224, 0x8000, v222
	v_add_u32_e32 v225, 0x8000, v223
	v_add_u32_e32 v228, 0x1000, v220
	v_add_u32_e32 v229, 64, v221
	s_add_u32 s60, s40, 0x0
	s_add_u32 s61, s40, 0x2000
	s_add_u32 s62, s40, 0x4000
	s_add_u32 s63, s40, 0x6000
	s_add_u32 s64, s40, 0x8000
	s_add_u32 s65, s40, 0xa000
	s_add_u32 s66, s40, 0xc000
	s_add_u32 s67, s40, 0xe000
	v_mov_b32_e32 v202, 0x12000
	s_branch .LBB3_3
.LBB3_1:
	s_load_dword s6, s[0:1], 0x0
	s_waitcnt lgkmcnt(0)
	s_add_i32 s2, s6, s2
	s_ashr_i32 s30, s2, 3
	s_ashr_i32 s31, s30, 31
	s_lshr_b32 s31, s31, 29
	s_lshl_b32 s6, s2, 4
	s_add_i32 s31, s30, s31
	s_and_b32 s6, s6, 0x70
	s_ashr_i32 s34, s31, 3
	s_and_b32 s31, s31, 0x1fffff8
	s_add_i32 s34, s6, s34
	s_mul_i32 s54, s34, 0x12000
	s_mul_hi_i32 s55, s34, 0x12000
	s_add_u32 s46, s50, s54
	s_addc_u32 s47, s51, s55
	s_add_u32 s48, s52, s54
	s_addc_u32 s49, s53, s55
	s_sub_i32 s6, s30, s31
	v_lshl_or_b32 v80, s6, 7, v192
	s_add_u32 s6, s40, 0x0
	v_mad_i64_i32 v[174:175], s[30:31], s34, v202, v[178:179]
	s_mov_b32 m0, s6
	s_add_u32 s6, s40, 0x8000
	v_mad_i64_i32 v[176:177], s[30:31], s34, v202, v[180:181]
	global_load_lds_dwordx4 v[174:175], off
	s_mov_b32 m0, s6
	s_add_u32 s6, s40, 0x2000
	global_load_lds_dwordx4 v[176:177], off
	v_lshl_add_u64 v[82:83], v[174:175], 0, s[8:9]
	s_mov_b32 m0, s6
	s_add_u32 s6, s40, 0x4000
	s_ashr_i32 s35, s34, 31
	global_load_lds_dwordx4 v[82:83], off
	v_lshl_add_u64 v[82:83], v[174:175], 0, s[10:11]
	s_mov_b32 m0, s6
	s_add_u32 s6, s40, 0xa000
	global_load_lds_dwordx4 v[82:83], off
	v_lshl_add_u64 v[82:83], v[176:177], 0, 64
	s_mov_b32 m0, s6
	s_lshl_b64 s[30:31], s[34:35], 10
	v_ashrrev_i32_e32 v81, 31, v80
	global_load_lds_dwordx4 v[82:83], off
	v_lshl_add_u64 v[82:83], s[30:31], 0, v[80:81]
	v_or_b32_e32 v82, v82, v168
	v_lshlrev_b64 v[82:83], 6, v[82:83]
	v_lshl_add_u64 v[82:83], v[182:183], 0, v[82:83]
	global_load_dwordx4 v[152:155], v[82:83], off nt
	global_load_dwordx4 v[156:159], v[82:83], off offset:16 nt
